# union1 + resid |x| row-max butterfly also replaced by DPP row max + readlane (all 18 ds_bpermute round trips per row gone in the XCD-local resid loops)
# baseline (speedup 1.0000x reference)
; __device__ __forceinline__ void resid_rows(bf16* X, const bf16* Y, const float* PART, const float* gpost, float* RSv, float* RQv, float* fout, unsigned char* XQv, int m0, int mstep, int lane, int M_end = M) {
;     ...
;         const float ps = wave_sum(cp); const float rs1 = 1.f / sqrtf(ps * (1.f / DM) + NORM_EPS);
;         f32x4 v[8]; float s = 0.f;
; #pragma unroll
;         for (int j = 0; j < 8; ++j) { const v2u x = cx[j], y = cy[j];
;             v[j].x = bflo(x.x) + bflo(y.x) * rs1 * g[j].x; v[j].y = bfhi(x.x) + bfhi(y.x) * rs1 * g[j].y; v[j].z = bflo(x.y) + bflo(y.y) * rs1 * g[j].z; v[j].w = bfhi(x.y) + bfhi(y.y) * rs1 * g[j].w;
;             s += (v[j].x * v[j].x + v[j].y * v[j].y) + (v[j].z * v[j].z + v[j].w * v[j].w); }
.LBB0_1027:
	s_nop 1
	v_add_f32_dpp v1, v108, v108 quad_perm:[1,0,3,2] row_mask:0xf bank_mask:0xf
	s_nop 1
	v_add_f32_dpp v1, v1, v1 quad_perm:[2,3,0,1] row_mask:0xf bank_mask:0xf
	s_nop 1
	v_add_f32_dpp v1, v1, v1 row_half_mirror row_mask:0xf bank_mask:0xf
	s_nop 1
	v_add_f32_dpp v1, v1, v1 row_mirror row_mask:0xf bank_mask:0xf
	s_nop 1
	v_readlane_b32 s100, v1, 0
	v_readlane_b32 s101, v1, 16
	s_nop 1
	v_mov_b32_e32 v210, s100
	v_add_f32_e32 v210, s101, v210
	v_readlane_b32 s100, v1, 32
	v_readlane_b32 s101, v1, 48
	s_nop 1
	v_add_f32_e32 v210, s100, v210
	v_add_f32_e32 v1, s101, v210
	v_lshlrev_b32_e32 v122, 16, v100
	v_and_b32_e32 v123, 0xffff0000, v100
	v_lshlrev_b32_e32 v124, 16, v101
	v_lshlrev_b32_e32 v118, 16, v104
	v_and_b32_e32 v119, 0xffff0000, v104
	v_lshlrev_b32_e32 v104, 16, v105
	v_and_b32_e32 v105, 0xffff0000, v105
	v_lshlrev_b32_e32 v108, 16, v106
	v_and_b32_e32 v109, 0xffff0000, v106
	v_lshlrev_b32_e32 v106, 16, v107
	v_and_b32_e32 v107, 0xffff0000, v107
	v_lshlrev_b32_e32 v120, 16, v102
	v_and_b32_e32 v121, 0xffff0000, v102
	v_lshlrev_b32_e32 v102, 16, v103
	v_and_b32_e32 v103, 0xffff0000, v103
	s_mov_b32 s3, 0x23800000
	v_fmamk_f32 v1, v1, 0x3a000000, v240
	v_mul_f32_e32 v2, 0x4f800000, v1
	v_cmp_gt_f32_e32 vcc, s82, v1
	s_nop 1
	v_cndmask_b32_e32 v1, v1, v2, vcc
	v_sqrt_f32_e32 v2, v1
	s_nop 0
	v_add_u32_e32 v100, -1, v2
	v_add_u32_e32 v117, 1, v2
	v_fma_f32 v125, -v100, v2, v1
	v_fma_f32 v126, -v117, v2, v1
	v_cmp_ge_f32_e64 s[42:43], 0, v125
	v_and_b32_e32 v125, 0xffff0000, v101
	s_nop 0
	v_cndmask_b32_e64 v2, v2, v100, s[42:43]
	v_cmp_lt_f32_e64 s[42:43], 0, v126
	s_nop 1
	v_cndmask_b32_e64 v2, v2, v117, s[42:43]
	v_mul_f32_e32 v100, 0x37800000, v2
	v_cndmask_b32_e32 v2, v2, v100, vcc
	v_cmp_class_f32_e32 vcc, v1, v241
	s_nop 1
	v_cndmask_b32_e32 v1, v2, v1, vcc
	v_div_scale_f32 v2, s[4:5], v1, v1, 1.0
	v_rcp_f32_e32 v100, v2
	v_div_scale_f32 v101, vcc, 1.0, v1, 1.0
	v_fma_f32 v117, -v2, v100, 1.0
	v_fmac_f32_e32 v100, v117, v100
	v_mul_f32_e32 v117, v101, v100
	v_fma_f32 v126, -v2, v117, v101
	v_fmac_f32_e32 v117, v126, v100
	v_fma_f32 v2, -v2, v117, v101
	v_div_fmas_f32 v2, v2, v100, v117
	v_div_fixup_f32 v2, v2, v1, 1.0
	v_pk_mul_f32 v[100:101], v[2:3], v[118:119] op_sel_hi:[0,1]
	v_pk_mul_f32 v[104:105], v[2:3], v[104:105] op_sel_hi:[0,1]
	v_pk_mul_f32 v[118:119], v[2:3], v[122:123] op_sel_hi:[0,1]
	v_pk_fma_f32 v[108:109], v[4:5], v[100:101], v[108:109]
	v_pk_fma_f32 v[106:107], v[6:7], v[104:105], v[106:107]
	v_pk_fma_f32 v[100:101], v[8:9], v[118:119], v[120:121]
	v_pk_mul_f32 v[104:105], v[2:3], v[124:125] op_sel_hi:[0,1]
	v_lshlrev_b32_e32 v118, 16, v96
	v_and_b32_e32 v119, 0xffff0000, v96
	v_pk_fma_f32 v[104:105], v[10:11], v[104:105], v[102:103]
	v_lshlrev_b32_e32 v102, 16, v98
	v_and_b32_e32 v103, 0xffff0000, v98
	v_pk_mul_f32 v[118:119], v[2:3], v[118:119] op_sel_hi:[0,1]
	v_lshlrev_b32_e32 v96, 16, v97
	v_and_b32_e32 v97, 0xffff0000, v97
	v_pk_fma_f32 v[102:103], v[12:13], v[118:119], v[102:103]
	v_lshlrev_b32_e32 v98, 16, v99
	v_and_b32_e32 v99, 0xffff0000, v99
	v_pk_mul_f32 v[96:97], v[2:3], v[96:97] op_sel_hi:[0,1]
	v_lshlrev_b32_e32 v118, 16, v92
	v_and_b32_e32 v119, 0xffff0000, v92
	v_pk_fma_f32 v[98:99], v[14:15], v[96:97], v[98:99]
	v_lshlrev_b32_e32 v96, 16, v94
	v_and_b32_e32 v97, 0xffff0000, v94
	v_pk_mul_f32 v[118:119], v[2:3], v[118:119] op_sel_hi:[0,1]
	v_lshlrev_b32_e32 v92, 16, v93
	v_and_b32_e32 v93, 0xffff0000, v93
	v_pk_fma_f32 v[96:97], v[16:17], v[118:119], v[96:97]
	v_lshlrev_b32_e32 v94, 16, v95
	v_and_b32_e32 v95, 0xffff0000, v95
	v_pk_mul_f32 v[92:93], v[2:3], v[92:93] op_sel_hi:[0,1]
	v_lshlrev_b32_e32 v118, 16, v88
	v_and_b32_e32 v119, 0xffff0000, v88
	v_pk_fma_f32 v[94:95], v[18:19], v[92:93], v[94:95]
	v_lshlrev_b32_e32 v92, 16, v90
	v_and_b32_e32 v93, 0xffff0000, v90
	v_pk_mul_f32 v[118:119], v[2:3], v[118:119] op_sel_hi:[0,1]
	v_lshlrev_b32_e32 v88, 16, v89
	v_and_b32_e32 v89, 0xffff0000, v89
	v_pk_fma_f32 v[92:93], v[20:21], v[118:119], v[92:93]
	v_lshlrev_b32_e32 v90, 16, v91
	v_and_b32_e32 v91, 0xffff0000, v91
	v_pk_mul_f32 v[88:89], v[2:3], v[88:89] op_sel_hi:[0,1]
	v_lshlrev_b32_e32 v118, 16, v84
	v_and_b32_e32 v119, 0xffff0000, v84
	v_pk_fma_f32 v[90:91], v[22:23], v[88:89], v[90:91]
	v_lshlrev_b32_e32 v88, 16, v86
	v_and_b32_e32 v89, 0xffff0000, v86
	v_pk_mul_f32 v[118:119], v[2:3], v[118:119] op_sel_hi:[0,1]
	v_lshlrev_b32_e32 v84, 16, v85
	v_and_b32_e32 v85, 0xffff0000, v85
	v_pk_fma_f32 v[88:89], v[24:25], v[118:119], v[88:89]
	v_lshlrev_b32_e32 v86, 16, v87
	v_and_b32_e32 v87, 0xffff0000, v87
	v_pk_mul_f32 v[84:85], v[2:3], v[84:85] op_sel_hi:[0,1]
	v_lshlrev_b32_e32 v118, 16, v80
	v_and_b32_e32 v119, 0xffff0000, v80
	v_pk_fma_f32 v[86:87], v[26:27], v[84:85], v[86:87]
	v_lshlrev_b32_e32 v84, 16, v82
	v_and_b32_e32 v85, 0xffff0000, v82
	v_pk_mul_f32 v[118:119], v[2:3], v[118:119] op_sel_hi:[0,1]
	v_lshlrev_b32_e32 v80, 16, v81
	v_and_b32_e32 v81, 0xffff0000, v81
	v_pk_fma_f32 v[84:85], v[28:29], v[118:119], v[84:85]
	v_lshlrev_b32_e32 v82, 16, v83
	v_and_b32_e32 v83, 0xffff0000, v83
	v_pk_mul_f32 v[80:81], v[2:3], v[80:81] op_sel_hi:[0,1]
	v_lshlrev_b32_e32 v118, 16, v76
	v_and_b32_e32 v119, 0xffff0000, v76
	v_lshlrev_b32_e32 v76, 16, v77
	v_and_b32_e32 v77, 0xffff0000, v77
	v_pk_fma_f32 v[82:83], v[30:31], v[80:81], v[82:83]
	v_lshlrev_b32_e32 v80, 16, v78
	v_and_b32_e32 v81, 0xffff0000, v78
	v_pk_mul_f32 v[118:119], v[2:3], v[118:119] op_sel_hi:[0,1]
	v_lshlrev_b32_e32 v78, 16, v79
	v_and_b32_e32 v79, 0xffff0000, v79
	v_pk_mul_f32 v[76:77], v[2:3], v[76:77] op_sel_hi:[0,1]
	v_pk_mul_f32 v[120:121], v[100:101], v[100:101]
	v_pk_mul_f32 v[122:123], v[104:105], v[104:105]
; #define GAS __attribute__((address_space(1)))
; __device__ __forceinline__ unsigned pk2(float lo, float hi) { f32x2_t_ v = {lo, hi}; bf16x2_t_ b = __builtin_convertvector(v, bf16x2_t_); return __builtin_bit_cast(unsigned, b); }
; __device__ __forceinline__ float quant_row(const f32x4 (&v)[8], unsigned char* xq, int lane) {
;     ...
;     for (int j = 0; j < 8; ++j) mx = __builtin_fmaxf(mx, __builtin_fmaxf(__builtin_fmaxf(__builtin_fabsf(v[j].x), __builtin_fabsf(v[j].y)), __builtin_fmaxf(__builtin_fabsf(v[j].z), __builtin_fabsf(v[j].w))));
;     mx = __builtin_fmaxf(wave_max(mx), 1e-20f);
; __device__ __forceinline__ void resid_rows(bf16* X, const bf16* Y, const float* PART, const float* gpost, float* RSv, float* RQv, float* fout, unsigned char* XQv, int m0, int mstep, int lane, int M_end = M) {
;     ...
;         for (int j = 0; j < 8; ++j) { const v2u x = cx[j], y = cy[j];
;             v[j].x = bflo(x.x) + bflo(y.x) * rs1 * g[j].x; v[j].y = bfhi(x.x) + bfhi(y.x) * rs1 * g[j].y; v[j].z = bflo(x.y) + bflo(y.y) * rs1 * g[j].z; v[j].w = bfhi(x.y) + bfhi(y.y) * rs1 * g[j].w;
;             s += (v[j].x * v[j].x + v[j].y * v[j].y) + (v[j].z * v[j].z + v[j].w * v[j].w); }
;         if (fout) { GAS f32x4* xo = (GAS f32x4*)(fout + (size_t)m * DM) + lane;
; #pragma unroll
;             for (int j = 0; j < 8; ++j) xo[64 * j] = v[j]; }
;         else { s = wave_sum(s); GAS v2u* xw = (GAS v2u*)(X + (size_t)m * DM) + lane;
; #pragma unroll
;             for (int j = 0; j < 8; ++j) { v2u w; w.x = pk2(v[j].x, v[j].y); w.y = pk2(v[j].z, v[j].w); xw[64 * j] = w; }
	v_pk_fma_f32 v[80:81], v[32:33], v[118:119], v[80:81]
	v_pk_fma_f32 v[76:77], v[34:35], v[76:77], v[78:79]
	v_pk_mul_f32 v[78:79], v[108:109], v[108:109]
	v_pk_mul_f32 v[118:119], v[106:107], v[106:107]
	v_add_f32_e32 v1, v123, v122
	v_add_f32_e32 v2, v120, v121
	v_add_f32_e32 v1, v2, v1
	v_add_f32_e32 v2, v119, v118
	v_add_f32_e32 v78, v78, v79
	v_pk_mul_f32 v[124:125], v[102:103], v[102:103]
	v_pk_mul_f32 v[126:127], v[98:99], v[98:99]
	v_add_f32_e32 v2, v78, v2
	v_add_f32_e32 v1, v2, v1
	v_add_f32_e32 v2, v127, v126
	v_add_f32_e32 v78, v124, v125
	v_pk_mul_f32 v[128:129], v[96:97], v[96:97]
	v_pk_mul_f32 v[130:131], v[94:95], v[94:95]
	v_add_f32_e32 v2, v78, v2
	v_add_f32_e32 v1, v2, v1
	v_add_f32_e32 v2, v131, v130
	v_add_f32_e32 v78, v128, v129
	v_pk_mul_f32 v[132:133], v[92:93], v[92:93]
	v_pk_mul_f32 v[134:135], v[90:91], v[90:91]
	v_add_f32_e32 v2, v78, v2
	v_add_f32_e32 v1, v2, v1
	v_add_f32_e32 v2, v135, v134
	v_add_f32_e32 v78, v132, v133
	v_pk_mul_f32 v[136:137], v[88:89], v[88:89]
	v_pk_mul_f32 v[138:139], v[86:87], v[86:87]
	v_add_f32_e32 v2, v78, v2
	v_add_f32_e32 v1, v2, v1
	v_add_f32_e32 v2, v139, v138
	v_add_f32_e32 v78, v136, v137
	v_pk_mul_f32 v[140:141], v[84:85], v[84:85]
	v_pk_mul_f32 v[142:143], v[82:83], v[82:83]
	v_add_f32_e32 v2, v78, v2
	v_add_f32_e32 v1, v2, v1
	v_add_f32_e32 v2, v143, v142
	v_add_f32_e32 v78, v140, v141
	v_pk_mul_f32 v[144:145], v[80:81], v[80:81]
	v_pk_mul_f32 v[146:147], v[76:77], v[76:77]
	v_add_f32_e32 v2, v78, v2
	v_add_f32_e32 v1, v2, v1
	v_add_f32_e32 v2, v147, v146
	v_add_f32_e32 v78, v144, v145
	v_add_f32_e32 v2, v78, v2
	v_add_f32_e32 v1, v2, v1
	s_nop 1
	v_add_f32_dpp v1, v1, v1 quad_perm:[1,0,3,2] row_mask:0xf bank_mask:0xf
	s_nop 1
	v_add_f32_dpp v1, v1, v1 quad_perm:[2,3,0,1] row_mask:0xf bank_mask:0xf
	s_nop 1
	v_add_f32_dpp v1, v1, v1 row_half_mirror row_mask:0xf bank_mask:0xf
	s_nop 1
	v_add_f32_dpp v1, v1, v1 row_mirror row_mask:0xf bank_mask:0xf
	s_nop 1
	v_readlane_b32 s100, v1, 0
	v_readlane_b32 s101, v1, 16
	s_nop 1
	v_mov_b32_e32 v210, s100
	v_add_f32_e32 v210, s101, v210
	v_readlane_b32 s100, v1, 32
	v_readlane_b32 s101, v1, 48
	s_nop 1
	v_add_f32_e32 v210, s100, v210
	v_add_f32_e32 v1, s101, v210
	v_max_f32_e64 v78, |v104|, |v105|
	v_max3_f32 v78, |v100|, |v101|, v78
	v_max_f32_e64 v79, |v94|, |v95|
	v_max3_f32 v79, |v96|, |v97|, v79
	v_cvt_pk_bf16_f32 v118, v108, v109
	v_cvt_pk_bf16_f32 v119, v106, v107
	v_max_f32_e64 v2, |v106|, |v107|
	v_max3_f32 v2, |v108|, |v109|, v2
	v_max3_f32 v2, v2, 0, v78
	v_max_f32_e64 v78, |v98|, |v99|
	v_max3_f32 v78, |v102|, |v103|, v78
	v_max3_f32 v2, v2, v78, v79
	v_max_f32_e64 v78, |v90|, |v91|
	v_max_f32_e64 v79, |v86|, |v87|
	v_max3_f32 v78, |v92|, |v93|, v78
	v_max3_f32 v79, |v88|, |v89|, v79
	v_max3_f32 v2, v2, v78, v79
	v_max_f32_e64 v78, |v82|, |v83|
	v_max_f32_e64 v79, |v76|, |v77|
	v_max3_f32 v78, |v84|, |v85|, v78
	v_max3_f32 v79, |v80|, |v81|, v79
	v_max3_f32 v117, v2, v78, v79
	s_nop 1
	v_max_f32_dpp v117, v117, v117 quad_perm:[1,0,3,2] row_mask:0xf bank_mask:0xf
	s_nop 1
	v_max_f32_dpp v117, v117, v117 quad_perm:[2,3,0,1] row_mask:0xf bank_mask:0xf
	s_nop 1
	v_max_f32_dpp v117, v117, v117 row_half_mirror row_mask:0xf bank_mask:0xf
	s_nop 1
	v_max_f32_dpp v117, v117, v117 row_mirror row_mask:0xf bank_mask:0xf
	s_nop 1
	v_readlane_b32 s100, v117, 0
	v_readlane_b32 s101, v117, 16
	s_nop 1
	v_mov_b32_e32 v210, s100
	v_max_f32_e32 v210, s101, v210
	v_readlane_b32 s100, v117, 32
	v_readlane_b32 s101, v117, 48
	s_nop 1
	v_max_f32_e32 v210, s100, v210
	v_max_f32_e32 v117, s101, v210
	v_lshl_add_u64 v[78:79], s[84:85], 0, v[38:39]
	s_waitcnt lgkmcnt(0)
	v_add_co_u32_e32 v120, vcc, s3, v78
	v_cvt_pk_bf16_f32 v78, v100, v101
	s_nop 0
	v_addc_co_u32_e32 v121, vcc, 0, v79, vcc
	s_waitcnt vmcnt(0)
	global_store_dwordx2 v[120:121], v[118:119], off
	s_waitcnt lgkmcnt(0)
	v_cvt_pk_bf16_f32 v79, v104, v105
	global_store_dwordx2 v[120:121], v[78:79], off offset:512
	v_cvt_pk_bf16_f32 v78, v102, v103
	v_cvt_pk_bf16_f32 v79, v98, v99
	global_store_dwordx2 v[120:121], v[78:79], off offset:1024
	s_waitcnt lgkmcnt(0)
	v_cvt_pk_bf16_f32 v78, v96, v97
	v_cvt_pk_bf16_f32 v79, v94, v95
	global_store_dwordx2 v[120:121], v[78:79], off offset:1536
	v_cvt_pk_bf16_f32 v78, v92, v93
	s_waitcnt lgkmcnt(0)
	v_cvt_pk_bf16_f32 v79, v90, v91
	global_store_dwordx2 v[120:121], v[78:79], off offset:2048
	v_cvt_pk_bf16_f32 v78, v88, v89
	v_cvt_pk_bf16_f32 v79, v86, v87
	s_waitcnt lgkmcnt(0)
	global_store_dwordx2 v[120:121], v[78:79], off offset:2560
	v_cvt_pk_bf16_f32 v78, v84, v85
	v_cvt_pk_bf16_f32 v79, v82, v83
	s_mov_b32 s3, 0x1e3ce508
	global_store_dwordx2 v[120:121], v[78:79], off offset:3072
	s_waitcnt lgkmcnt(0)
; #define GAS __attribute__((address_space(1)))
; __device__ __forceinline__ float quant_row(const f32x4 (&v)[8], unsigned char* xq, int lane) {
;     ...
;     mx = __builtin_fmaxf(wave_max(mx), 1e-20f);
;     const float q = 127.0f / mx;
;     GAS unsigned* o4 = (GAS unsigned*)xq + lane;
; #pragma unroll
;     for (int j = 0; j < 8; ++j) o4[64 * j] = q4(v[j], q);
;     return mx * (1.0f / 127.0f);
; __device__ __forceinline__ void resid_rows(bf16* X, const bf16* Y, const float* PART, const float* gpost, float* RSv, float* RQv, float* fout, unsigned char* XQv, int m0, int mstep, int lane, int M_end = M) {
;     ...
;             const float dq = quant_row(v, XQv + (size_t)m * DM, lane);
;             if (lane == 0) { const float r = 1.f / sqrtf(s * (1.f / DM) + NORM_EPS); RSv[m] = r; RQv[m] = r * dq; } }
	v_max_f32_e32 v78, s3, v117
	s_mov_b32 s3, 0x42fe0000
	v_div_scale_f32 v79, s[4:5], v78, v78, s3
	v_rcp_f32_e32 v117, v79
	v_cvt_pk_bf16_f32 v118, v80, v81
	v_cvt_pk_bf16_f32 v119, v76, v77
	global_store_dwordx2 v[120:121], v[118:119], off offset:3584
	v_fma_f32 v118, -v79, v117, 1.0
	v_fmac_f32_e32 v117, v118, v117
	v_div_scale_f32 v118, vcc, s3, v78, s3
	v_mul_f32_e32 v119, v118, v117
	v_fma_f32 v120, -v79, v119, v118
	v_fmac_f32_e32 v119, v120, v117
	v_fma_f32 v79, -v79, v119, v118
	v_div_fmas_f32 v79, v79, v117, v119
	v_div_fixup_f32 v79, v79, v78, s3
	v_mul_f32_e32 v109, v109, v79
	v_mul_f32_e32 v108, v108, v79
	v_rndne_f32_e32 v109, v109
	v_mul_f32_e32 v106, v106, v79
	v_mul_f32_e32 v107, v107, v79
	v_mul_f32_e32 v101, v101, v79
	v_rndne_f32_e32 v108, v108
	v_cvt_i32_f32_e32 v109, v109
	v_rndne_f32_e32 v106, v106
	v_rndne_f32_e32 v107, v107
	v_mul_f32_e32 v100, v100, v79
	v_rndne_f32_e32 v101, v101
	v_mul_f32_e32 v104, v104, v79
	v_mul_f32_e32 v105, v105, v79
	v_cvt_i32_f32_e32 v108, v108
	v_cvt_i32_f32_sdwa v106, v106 dst_sel:WORD_1 dst_unused:UNUSED_PAD src0_sel:DWORD
	v_cvt_i32_f32_e32 v107, v107
	v_rndne_f32_e32 v100, v100
	v_cvt_i32_f32_e32 v101, v101
	v_rndne_f32_e32 v104, v104
	v_rndne_f32_e32 v105, v105
	v_cvt_i32_f32_e32 v100, v100
	v_cvt_i32_f32_sdwa v104, v104 dst_sel:WORD_1 dst_unused:UNUSED_PAD src0_sel:DWORD
	v_cvt_i32_f32_e32 v105, v105
	v_lshlrev_b32_e32 v109, 8, v109
	v_lshl_add_u64 v[118:119], s[84:85], 0, v[36:37]
	v_and_b32_e32 v109, 0xff00, v109
	v_and_b32_e32 v106, 0xff0000, v106
	v_perm_b32 v107, v107, v108, s17
	s_mov_b32 s3, 0x8800000
	v_lshlrev_b32_e32 v101, 8, v101
	v_or3_b32 v108, v107, v109, v106
	v_add_co_u32_e32 v106, vcc, s3, v118
	v_and_b32_e32 v101, 0xff00, v101
	v_and_b32_e32 v104, 0xff0000, v104
	v_perm_b32 v100, v105, v100, s17
	v_addc_co_u32_e32 v107, vcc, 0, v119, vcc
	v_or3_b32 v100, v100, v101, v104
	v_mul_f32_e32 v101, v103, v79
	v_mul_f32_e32 v97, v97, v79
	v_mul_f32_e32 v93, v93, v79
	v_mul_f32_e32 v89, v89, v79
	v_mul_f32_e32 v85, v85, v79
	v_mul_f32_e32 v81, v81, v79
	global_store_dword v[106:107], v100, off offset:256
	v_mul_f32_e32 v100, v102, v79
	v_rndne_f32_e32 v101, v101
	v_mul_f32_e32 v98, v98, v79
	v_mul_f32_e32 v99, v99, v79
	v_mul_f32_e32 v96, v96, v79
	v_rndne_f32_e32 v97, v97
	v_mul_f32_e32 v94, v94, v79
	v_mul_f32_e32 v95, v95, v79
	v_mul_f32_e32 v92, v92, v79
	v_rndne_f32_e32 v93, v93
	v_mul_f32_e32 v90, v90, v79
	v_mul_f32_e32 v91, v91, v79
	v_mul_f32_e32 v88, v88, v79
	v_rndne_f32_e32 v89, v89
	v_mul_f32_e32 v86, v86, v79
	v_mul_f32_e32 v87, v87, v79
	v_mul_f32_e32 v84, v84, v79
	v_rndne_f32_e32 v85, v85
	v_mul_f32_e32 v82, v82, v79
	v_mul_f32_e32 v83, v83, v79
	v_mul_f32_e32 v80, v80, v79
	v_rndne_f32_e32 v81, v81
	v_mul_f32_e32 v76, v76, v79
	v_mul_f32_e32 v77, v77, v79
	v_rndne_f32_e32 v100, v100
	v_cvt_i32_f32_e32 v101, v101
	v_rndne_f32_e32 v98, v98
	v_rndne_f32_e32 v99, v99
	v_rndne_f32_e32 v96, v96
	v_cvt_i32_f32_e32 v97, v97
	v_rndne_f32_e32 v94, v94
	v_rndne_f32_e32 v95, v95
	v_rndne_f32_e32 v92, v92
	v_cvt_i32_f32_e32 v93, v93
	v_rndne_f32_e32 v90, v90
	v_rndne_f32_e32 v91, v91
	v_rndne_f32_e32 v88, v88
	v_cvt_i32_f32_e32 v89, v89
	v_rndne_f32_e32 v86, v86
	v_rndne_f32_e32 v87, v87
	v_rndne_f32_e32 v84, v84
	v_cvt_i32_f32_e32 v85, v85
	v_rndne_f32_e32 v82, v82
	v_rndne_f32_e32 v83, v83
	v_rndne_f32_e32 v80, v80
	v_cvt_i32_f32_e32 v81, v81
	v_rndne_f32_e32 v76, v76
	v_rndne_f32_e32 v77, v77
	v_cvt_i32_f32_e32 v100, v100
	v_cvt_i32_f32_sdwa v98, v98 dst_sel:WORD_1 dst_unused:UNUSED_PAD src0_sel:DWORD
	v_cvt_i32_f32_e32 v99, v99
	v_cvt_i32_f32_e32 v96, v96
	v_cvt_i32_f32_sdwa v94, v94 dst_sel:WORD_1 dst_unused:UNUSED_PAD src0_sel:DWORD
	v_cvt_i32_f32_e32 v95, v95
	v_cvt_i32_f32_e32 v92, v92
	v_cvt_i32_f32_sdwa v90, v90 dst_sel:WORD_1 dst_unused:UNUSED_PAD src0_sel:DWORD
	v_cvt_i32_f32_e32 v91, v91
	v_cvt_i32_f32_e32 v88, v88
	v_cvt_i32_f32_sdwa v86, v86 dst_sel:WORD_1 dst_unused:UNUSED_PAD src0_sel:DWORD
	v_cvt_i32_f32_e32 v87, v87
	v_cvt_i32_f32_e32 v84, v84
	v_cvt_i32_f32_sdwa v82, v82 dst_sel:WORD_1 dst_unused:UNUSED_PAD src0_sel:DWORD
	v_cvt_i32_f32_e32 v83, v83
	v_cvt_i32_f32_e32 v80, v80
	v_cvt_i32_f32_sdwa v76, v76 dst_sel:WORD_1 dst_unused:UNUSED_PAD src0_sel:DWORD
	v_cvt_i32_f32_e32 v77, v77
	v_lshlrev_b32_e32 v101, 8, v101
	v_lshlrev_b32_e32 v97, 8, v97
	v_lshlrev_b32_e32 v93, 8, v93
	v_lshlrev_b32_e32 v89, 8, v89
	v_lshlrev_b32_e32 v85, 8, v85
	v_lshlrev_b32_e32 v79, 8, v81
	v_and_b32_e32 v101, 0xff00, v101
	v_and_b32_e32 v98, 0xff0000, v98
	v_perm_b32 v99, v99, v100, s17
	v_and_b32_e32 v97, 0xff00, v97
	v_and_b32_e32 v94, 0xff0000, v94
	v_perm_b32 v95, v95, v96, s17
	v_and_b32_e32 v93, 0xff00, v93
	v_and_b32_e32 v90, 0xff0000, v90
	v_perm_b32 v91, v91, v92, s17
	v_and_b32_e32 v89, 0xff00, v89
	v_and_b32_e32 v86, 0xff0000, v86
	v_perm_b32 v87, v87, v88, s17
	v_and_b32_e32 v85, 0xff00, v85
	v_and_b32_e32 v82, 0xff0000, v82
	v_perm_b32 v83, v83, v84, s17
	v_and_b32_e32 v79, 0xff00, v79
	v_and_b32_e32 v76, 0xff0000, v76
	v_perm_b32 v77, v77, v80, s17
	v_or3_b32 v98, v99, v101, v98
	v_or3_b32 v94, v95, v97, v94
	v_or3_b32 v90, v91, v93, v90
	v_or3_b32 v86, v87, v89, v86
	v_or3_b32 v82, v83, v85, v82
	v_or3_b32 v76, v77, v79, v76
	global_store_dword v[106:107], v108, off
	global_store_dword v[106:107], v98, off offset:512
	global_store_dword v[106:107], v94, off offset:768
	global_store_dword v[106:107], v90, off offset:1024
	global_store_dword v[106:107], v86, off offset:1280
	global_store_dword v[106:107], v82, off offset:1536
	global_store_dword v[106:107], v76, off offset:1792
	s_and_saveexec_b64 s[48:49], s[40:41]
	s_cbranch_execz .LBB0_1022
	v_fmamk_f32 v1, v1, 0x3a000000, v240
	v_mul_f32_e32 v2, 0x4f800000, v1
	v_cmp_gt_f32_e32 vcc, s82, v1
	s_nop 1
	v_cndmask_b32_e32 v1, v1, v2, vcc
	v_sqrt_f32_e32 v2, v1
	s_nop 0
	v_add_u32_e32 v76, -1, v2
	v_fma_f32 v79, -v76, v2, v1
	v_add_u32_e32 v77, 1, v2
	v_cmp_ge_f32_e64 s[42:43], 0, v79
	s_nop 1
	v_cndmask_b32_e64 v76, v2, v76, s[42:43]
	v_fma_f32 v2, -v77, v2, v1
	v_cmp_lt_f32_e64 s[42:43], 0, v2
	s_nop 1
	v_cndmask_b32_e64 v2, v76, v77, s[42:43]
	v_mul_f32_e32 v76, 0x37800000, v2
	v_cndmask_b32_e32 v2, v2, v76, vcc
	v_cmp_class_f32_e32 vcc, v1, v241
	v_mul_f32_e32 v77, 0x3c010204, v78
	s_nop 0
	v_cndmask_b32_e32 v1, v2, v1, vcc
	v_div_scale_f32 v2, s[4:5], v1, v1, 1.0
	v_rcp_f32_e32 v76, v2
	s_add_u32 s4, s84, s44
	s_addc_u32 s5, s85, s45
	v_fma_f32 v78, -v2, v76, 1.0
	v_fmac_f32_e32 v76, v78, v76
	v_div_scale_f32 v78, vcc, 1.0, v1, 1.0
	v_mul_f32_e32 v79, v78, v76
	v_fma_f32 v80, -v2, v79, v78
	v_fmac_f32_e32 v79, v80, v76
	v_fma_f32 v2, -v2, v79, v78
	v_div_fmas_f32 v2, v2, v76, v79
	v_div_fixup_f32 v1, v2, v1, 1.0
	global_store_dword v236, v1, s[4:5]
	v_mul_f32_e32 v1, v77, v1
	global_store_dword v237, v1, s[4:5]
	s_branch .LBB0_1022

; #define GAS __attribute__((address_space(1)))
; __device__ __forceinline__ unsigned pk2(float lo, float hi) { f32x2_t_ v = {lo, hi}; bf16x2_t_ b = __builtin_convertvector(v, bf16x2_t_); return __builtin_bit_cast(unsigned, b); }
; __device__ __forceinline__ float quant_row(const f32x4 (&v)[8], unsigned char* xq, int lane) {
;     ...
;     for (int j = 0; j < 8; ++j) mx = __builtin_fmaxf(mx, __builtin_fmaxf(__builtin_fmaxf(__builtin_fabsf(v[j].x), __builtin_fabsf(v[j].y)), __builtin_fmaxf(__builtin_fabsf(v[j].z), __builtin_fabsf(v[j].w))));
;     mx = __builtin_fmaxf(wave_max(mx), 1e-20f);
; __device__ __forceinline__ void resid_rows(bf16* X, const bf16* Y, const float* PART, const float* gpost, float* RSv, float* RQv, float* fout, unsigned char* XQv, int m0, int mstep, int lane, int M_end = M) {
;     ...
;             s += (v[j].x * v[j].x + v[j].y * v[j].y) + (v[j].z * v[j].z + v[j].w * v[j].w); }
;         if (fout) { GAS f32x4* xo = (GAS f32x4*)(fout + (size_t)m * DM) + lane;
; #pragma unroll
;             for (int j = 0; j < 8; ++j) xo[64 * j] = v[j]; }
;         else { s = wave_sum(s); GAS v2u* xw = (GAS v2u*)(X + (size_t)m * DM) + lane;
; #pragma unroll
;             for (int j = 0; j < 8; ++j) { v2u w; w.x = pk2(v[j].x, v[j].y); w.y = pk2(v[j].z, v[j].w); xw[64 * j] = w; }
.LBB0_1370:
.LBB0_1371:
	v_pk_mul_f32 v[122:123], v[40:41], v[40:41]
	v_pk_mul_f32 v[124:125], v[42:43], v[42:43]
	v_pk_mul_f32 v[110:111], v[36:37], v[36:37]
	v_pk_mul_f32 v[120:121], v[38:39], v[38:39]
	v_add_f32_e32 v1, v125, v124
	v_add_f32_e32 v2, v122, v123
	v_add_f32_e32 v1, v2, v1
	v_add_f32_e32 v2, v121, v120
	v_add_f32_e32 v110, v110, v111
	v_pk_mul_f32 v[126:127], v[44:45], v[44:45]
	v_pk_mul_f32 v[128:129], v[46:47], v[46:47]
	v_add_f32_e32 v2, v110, v2
	v_add_f32_e32 v1, v2, v1
	v_add_f32_e32 v2, v129, v128
	v_add_f32_e32 v110, v126, v127
	v_pk_mul_f32 v[130:131], v[48:49], v[48:49]
	v_pk_mul_f32 v[132:133], v[50:51], v[50:51]
	v_add_f32_e32 v2, v110, v2
	v_add_f32_e32 v1, v2, v1
	v_add_f32_e32 v2, v133, v132
	v_add_f32_e32 v110, v130, v131
	v_pk_mul_f32 v[134:135], v[52:53], v[52:53]
	v_pk_mul_f32 v[136:137], v[54:55], v[54:55]
	v_add_f32_e32 v2, v110, v2
	v_add_f32_e32 v1, v2, v1
	v_add_f32_e32 v2, v137, v136
	v_add_f32_e32 v110, v134, v135
	v_pk_mul_f32 v[138:139], v[56:57], v[56:57]
	v_pk_mul_f32 v[140:141], v[58:59], v[58:59]
	v_add_f32_e32 v2, v110, v2
	v_add_f32_e32 v1, v2, v1
	v_add_f32_e32 v2, v141, v140
	v_add_f32_e32 v110, v138, v139
	v_pk_mul_f32 v[142:143], v[60:61], v[60:61]
	v_pk_mul_f32 v[144:145], v[62:63], v[62:63]
	v_add_f32_e32 v2, v110, v2
	v_add_f32_e32 v1, v2, v1
	v_add_f32_e32 v2, v145, v144
	v_add_f32_e32 v110, v142, v143
	v_pk_mul_f32 v[146:147], v[64:65], v[64:65]
	v_pk_mul_f32 v[148:149], v[66:67], v[66:67]
	v_add_f32_e32 v2, v110, v2
	v_add_f32_e32 v1, v2, v1
	v_add_f32_e32 v2, v149, v148
	v_add_f32_e32 v110, v146, v147
	v_add_f32_e32 v2, v110, v2
	v_add_f32_e32 v1, v2, v1
	s_nop 1
	v_add_f32_dpp v1, v1, v1 quad_perm:[1,0,3,2] row_mask:0xf bank_mask:0xf
	s_nop 1
	v_add_f32_dpp v1, v1, v1 quad_perm:[2,3,0,1] row_mask:0xf bank_mask:0xf
	s_nop 1
	v_add_f32_dpp v1, v1, v1 row_half_mirror row_mask:0xf bank_mask:0xf
	s_nop 1
	v_add_f32_dpp v1, v1, v1 row_mirror row_mask:0xf bank_mask:0xf
	s_nop 1
	v_readlane_b32 s100, v1, 0
	v_readlane_b32 s101, v1, 16
	s_nop 1
	v_mov_b32_e32 v210, s100
	v_add_f32_e32 v210, s101, v210
	v_readlane_b32 s100, v1, 32
	v_readlane_b32 s101, v1, 48
	s_nop 1
	v_add_f32_e32 v210, s100, v210
	v_add_f32_e32 v1, s101, v210
	v_max_f32_e64 v110, |v38|, |v38|
	v_max_f32_e64 v111, |v42|, |v42|
	v_max_f32_e64 v119, |v50|, |v50|
	s_mov_b32 s0, 0x23800000
	v_cvt_pk_bf16_f32 v120, v36, v37
	v_cvt_pk_bf16_f32 v121, v38, v39
	v_max_f32_e64 v2, |v39|, |v39|
	v_max_f32_e32 v2, v110, v2
	v_max_f32_e64 v110, |v43|, |v43|
	v_max_f32_e32 v110, v111, v110
	v_max3_f32 v2, |v36|, |v37|, v2
	v_max3_f32 v110, |v40|, |v41|, v110
	v_max3_f32 v2, v2, 0, v110
	v_max_f32_e64 v110, |v47|, |v47|
	v_max_f32_e64 v111, |v46|, |v46|
	v_max_f32_e32 v110, v111, v110
	v_max_f32_e64 v111, |v51|, |v51|
	v_max_f32_e32 v111, v119, v111
	v_max3_f32 v110, |v44|, |v45|, v110
	v_max3_f32 v111, |v48|, |v49|, v111
	v_max3_f32 v2, v2, v110, v111
	v_max_f32_e64 v110, |v55|, |v55|
	v_max_f32_e64 v111, |v54|, |v54|
	v_max_f32_e32 v110, v111, v110
	v_max_f32_e64 v111, |v59|, |v59|
	v_max_f32_e64 v119, |v58|, |v58|
	v_max_f32_e32 v111, v119, v111
	v_max3_f32 v110, |v52|, |v53|, v110
	v_max3_f32 v111, |v56|, |v57|, v111
	v_max3_f32 v2, v2, v110, v111
	v_max_f32_e64 v110, |v63|, |v63|
	v_max_f32_e64 v111, |v62|, |v62|
	v_max_f32_e32 v110, v111, v110
	v_max_f32_e64 v111, |v67|, |v67|
	v_max_f32_e64 v119, |v66|, |v66|
	v_max_f32_e32 v111, v119, v111
	v_max3_f32 v110, |v60|, |v61|, v110
	v_max3_f32 v111, |v64|, |v65|, v111
	v_max3_f32 v119, v2, v110, v111
	s_nop 1
	v_max_f32_dpp v119, v119, v119 quad_perm:[1,0,3,2] row_mask:0xf bank_mask:0xf
	s_nop 1
	v_max_f32_dpp v119, v119, v119 quad_perm:[2,3,0,1] row_mask:0xf bank_mask:0xf
	s_nop 1
	v_max_f32_dpp v119, v119, v119 row_half_mirror row_mask:0xf bank_mask:0xf
	s_nop 1
	v_max_f32_dpp v119, v119, v119 row_mirror row_mask:0xf bank_mask:0xf
	s_nop 1
	v_readlane_b32 s100, v119, 0
	v_readlane_b32 s101, v119, 16
	s_nop 1
	v_mov_b32_e32 v210, s100
	v_max_f32_e32 v210, s101, v210
	v_readlane_b32 s100, v119, 32
	v_readlane_b32 s101, v119, 48
	s_nop 1
	v_max_f32_e32 v210, s100, v210
	v_max_f32_e32 v119, s101, v210
	v_lshl_add_u64 v[110:111], s[84:85], 0, v[70:71]
	s_waitcnt lgkmcnt(0)
	v_add_co_u32_e32 v122, vcc, s0, v110
	v_cvt_pk_bf16_f32 v110, v40, v41
	s_nop 0
	v_addc_co_u32_e32 v123, vcc, 0, v111, vcc
	global_store_dwordx2 v[122:123], v[120:121], off
	s_waitcnt lgkmcnt(0)
	v_cvt_pk_bf16_f32 v111, v42, v43
	global_store_dwordx2 v[122:123], v[110:111], off offset:512
	v_cvt_pk_bf16_f32 v110, v44, v45
	v_cvt_pk_bf16_f32 v111, v46, v47
	global_store_dwordx2 v[122:123], v[110:111], off offset:1024
	s_waitcnt lgkmcnt(0)
	v_cvt_pk_bf16_f32 v110, v48, v49
	v_cvt_pk_bf16_f32 v111, v50, v51
	global_store_dwordx2 v[122:123], v[110:111], off offset:1536
	v_cvt_pk_bf16_f32 v110, v52, v53
	s_waitcnt lgkmcnt(0)
	v_cvt_pk_bf16_f32 v111, v54, v55
	global_store_dwordx2 v[122:123], v[110:111], off offset:2048
	v_cvt_pk_bf16_f32 v110, v56, v57
	v_cvt_pk_bf16_f32 v111, v58, v59
	s_waitcnt lgkmcnt(0)
	global_store_dwordx2 v[122:123], v[110:111], off offset:2560
	v_cvt_pk_bf16_f32 v110, v60, v61
	v_cvt_pk_bf16_f32 v111, v62, v63
	s_mov_b32 s0, 0x1e3ce508
	global_store_dwordx2 v[122:123], v[110:111], off offset:3072
	s_waitcnt lgkmcnt(0)
; #define GAS __attribute__((address_space(1)))
; __device__ __forceinline__ float quant_row(const f32x4 (&v)[8], unsigned char* xq, int lane) {
;     ...
;     mx = __builtin_fmaxf(wave_max(mx), 1e-20f);
;     const float q = 127.0f / mx;
;     GAS unsigned* o4 = (GAS unsigned*)xq + lane;
; #pragma unroll
;     for (int j = 0; j < 8; ++j) o4[64 * j] = q4(v[j], q);
;     return mx * (1.0f / 127.0f);
; __device__ __forceinline__ void resid_rows(bf16* X, const bf16* Y, const float* PART, const float* gpost, float* RSv, float* RQv, float* fout, unsigned char* XQv, int m0, int mstep, int lane, int M_end = M) {
;     ...
;             const float dq = quant_row(v, XQv + (size_t)m * DM, lane);
;             if (lane == 0) { const float r = 1.f / sqrtf(s * (1.f / DM) + NORM_EPS); RSv[m] = r; RQv[m] = r * dq; } }
	v_max_f32_e32 v110, s0, v119
	s_mov_b32 s0, 0x42fe0000
	v_div_scale_f32 v111, s[18:19], v110, v110, s0
	v_rcp_f32_e32 v119, v111
	v_cvt_pk_bf16_f32 v120, v64, v65
	v_cvt_pk_bf16_f32 v121, v66, v67
	global_store_dwordx2 v[122:123], v[120:121], off offset:3584
	v_fma_f32 v120, -v111, v119, 1.0
	v_fmac_f32_e32 v119, v120, v119
	v_div_scale_f32 v120, vcc, s0, v110, s0
	v_mul_f32_e32 v121, v120, v119
	v_fma_f32 v122, -v111, v121, v120
	v_fmac_f32_e32 v121, v122, v119
	v_fma_f32 v111, -v111, v121, v120
	v_div_fmas_f32 v111, v111, v119, v121
	v_div_fixup_f32 v111, v111, v110, s0
	v_mul_f32_e32 v37, v37, v111
	v_mul_f32_e32 v36, v36, v111
	v_rndne_f32_e32 v37, v37
	v_mul_f32_e32 v38, v38, v111
	v_mul_f32_e32 v39, v39, v111
	v_rndne_f32_e32 v36, v36
	v_cvt_i32_f32_e32 v37, v37
	v_rndne_f32_e32 v38, v38
	v_rndne_f32_e32 v39, v39
	v_cvt_i32_f32_e32 v36, v36
	v_cvt_i32_f32_sdwa v38, v38 dst_sel:WORD_1 dst_unused:UNUSED_PAD src0_sel:DWORD
	v_cvt_i32_f32_e32 v39, v39
	v_lshlrev_b32_e32 v37, 8, v37
	v_lshl_add_u64 v[120:121], s[84:85], 0, v[68:69]
	v_and_b32_e32 v37, 0xff00, v37
	v_and_b32_e32 v38, 0xff0000, v38
	v_perm_b32 v36, v39, v36, s17
	s_mov_b32 s0, 0x8800000
	v_or3_b32 v38, v36, v37, v38
	v_add_co_u32_e32 v36, vcc, s0, v120
	v_mul_f32_e32 v39, v41, v111
	s_nop 0
	v_addc_co_u32_e32 v37, vcc, 0, v121, vcc
	global_store_dword v[36:37], v38, off
	v_mul_f32_e32 v38, v40, v111
	v_rndne_f32_e32 v39, v39
	v_mul_f32_e32 v40, v42, v111
	v_mul_f32_e32 v41, v43, v111
	v_rndne_f32_e32 v38, v38
	v_cvt_i32_f32_e32 v39, v39
	v_rndne_f32_e32 v40, v40
	v_rndne_f32_e32 v41, v41
	v_cvt_i32_f32_e32 v38, v38
	v_cvt_i32_f32_sdwa v40, v40 dst_sel:WORD_1 dst_unused:UNUSED_PAD src0_sel:DWORD
	v_cvt_i32_f32_e32 v41, v41
	v_lshlrev_b32_e32 v39, 8, v39
	v_and_b32_e32 v39, 0xff00, v39
	v_and_b32_e32 v40, 0xff0000, v40
	v_perm_b32 v38, v41, v38, s17
	v_or3_b32 v38, v38, v39, v40
	v_mul_f32_e32 v39, v45, v111
	global_store_dword v[36:37], v38, off offset:256
	v_mul_f32_e32 v38, v44, v111
	v_rndne_f32_e32 v39, v39
	v_mul_f32_e32 v40, v46, v111
	v_mul_f32_e32 v41, v47, v111
	v_rndne_f32_e32 v38, v38
	v_cvt_i32_f32_e32 v39, v39
	v_rndne_f32_e32 v40, v40
	v_rndne_f32_e32 v41, v41
	v_cvt_i32_f32_e32 v38, v38
	v_cvt_i32_f32_sdwa v40, v40 dst_sel:WORD_1 dst_unused:UNUSED_PAD src0_sel:DWORD
	v_cvt_i32_f32_e32 v41, v41
	v_lshlrev_b32_e32 v39, 8, v39
	v_and_b32_e32 v39, 0xff00, v39
	v_and_b32_e32 v40, 0xff0000, v40
	v_perm_b32 v38, v41, v38, s17
	v_or3_b32 v38, v38, v39, v40
	v_mul_f32_e32 v39, v49, v111
	global_store_dword v[36:37], v38, off offset:512
	v_mul_f32_e32 v38, v48, v111
	v_rndne_f32_e32 v39, v39
	v_mul_f32_e32 v40, v50, v111
	v_mul_f32_e32 v41, v51, v111
	v_rndne_f32_e32 v38, v38
	v_cvt_i32_f32_e32 v39, v39
	v_rndne_f32_e32 v40, v40
	v_rndne_f32_e32 v41, v41
	v_cvt_i32_f32_e32 v38, v38
	v_cvt_i32_f32_sdwa v40, v40 dst_sel:WORD_1 dst_unused:UNUSED_PAD src0_sel:DWORD
	v_cvt_i32_f32_e32 v41, v41
	v_lshlrev_b32_e32 v39, 8, v39
	v_and_b32_e32 v39, 0xff00, v39
	v_and_b32_e32 v40, 0xff0000, v40
	v_perm_b32 v38, v41, v38, s17
	v_or3_b32 v38, v38, v39, v40
	v_mul_f32_e32 v39, v53, v111
	global_store_dword v[36:37], v38, off offset:768
	v_mul_f32_e32 v38, v52, v111
	v_rndne_f32_e32 v39, v39
	v_mul_f32_e32 v40, v54, v111
	v_mul_f32_e32 v41, v55, v111
	v_rndne_f32_e32 v38, v38
	v_cvt_i32_f32_e32 v39, v39
	v_rndne_f32_e32 v40, v40
	v_rndne_f32_e32 v41, v41
	v_cvt_i32_f32_e32 v38, v38
	v_cvt_i32_f32_sdwa v40, v40 dst_sel:WORD_1 dst_unused:UNUSED_PAD src0_sel:DWORD
	v_cvt_i32_f32_e32 v41, v41
	v_lshlrev_b32_e32 v39, 8, v39
	v_and_b32_e32 v39, 0xff00, v39
	v_and_b32_e32 v40, 0xff0000, v40
	v_perm_b32 v38, v41, v38, s17
	v_or3_b32 v38, v38, v39, v40
	v_mul_f32_e32 v39, v57, v111
	global_store_dword v[36:37], v38, off offset:1024
	v_mul_f32_e32 v38, v56, v111
	v_rndne_f32_e32 v39, v39
	v_mul_f32_e32 v40, v58, v111
	v_mul_f32_e32 v41, v59, v111
	v_rndne_f32_e32 v38, v38
	v_cvt_i32_f32_e32 v39, v39
	v_rndne_f32_e32 v40, v40
	v_rndne_f32_e32 v41, v41
	v_cvt_i32_f32_e32 v38, v38
	v_cvt_i32_f32_sdwa v40, v40 dst_sel:WORD_1 dst_unused:UNUSED_PAD src0_sel:DWORD
	v_cvt_i32_f32_e32 v41, v41
	v_lshlrev_b32_e32 v39, 8, v39
	v_and_b32_e32 v39, 0xff00, v39
	v_and_b32_e32 v40, 0xff0000, v40
	v_perm_b32 v38, v41, v38, s17
	v_or3_b32 v38, v38, v39, v40
	v_mul_f32_e32 v39, v61, v111
	global_store_dword v[36:37], v38, off offset:1280
	v_mul_f32_e32 v38, v60, v111
	v_rndne_f32_e32 v39, v39
	v_mul_f32_e32 v40, v62, v111
	v_mul_f32_e32 v41, v63, v111
	v_rndne_f32_e32 v38, v38
	v_cvt_i32_f32_e32 v39, v39
	v_rndne_f32_e32 v40, v40
	v_rndne_f32_e32 v41, v41
	v_cvt_i32_f32_e32 v38, v38
	v_cvt_i32_f32_sdwa v40, v40 dst_sel:WORD_1 dst_unused:UNUSED_PAD src0_sel:DWORD
	v_cvt_i32_f32_e32 v41, v41
	v_lshlrev_b32_e32 v39, 8, v39
	v_and_b32_e32 v39, 0xff00, v39
	v_and_b32_e32 v40, 0xff0000, v40
	v_perm_b32 v38, v41, v38, s17
	v_or3_b32 v38, v38, v39, v40
	v_mul_f32_e32 v39, v65, v111
	global_store_dword v[36:37], v38, off offset:1536
	v_mul_f32_e32 v38, v64, v111
	v_rndne_f32_e32 v39, v39
	v_mul_f32_e32 v40, v66, v111
	v_mul_f32_e32 v41, v67, v111
	v_rndne_f32_e32 v38, v38
	v_cvt_i32_f32_e32 v39, v39
	v_rndne_f32_e32 v40, v40
	v_rndne_f32_e32 v41, v41
	v_cvt_i32_f32_e32 v38, v38
	v_cvt_i32_f32_sdwa v40, v40 dst_sel:WORD_1 dst_unused:UNUSED_PAD src0_sel:DWORD
	v_cvt_i32_f32_e32 v41, v41
	v_lshlrev_b32_e32 v39, 8, v39
	v_and_b32_e32 v39, 0xff00, v39
	v_and_b32_e32 v40, 0xff0000, v40
	v_perm_b32 v38, v41, v38, s17
	v_or3_b32 v38, v38, v39, v40
	global_store_dword v[36:37], v38, off offset:1792
	s_and_saveexec_b64 s[48:49], s[38:39]
	s_cbranch_execz .LBB0_1362
	v_fmamk_f32 v1, v1, 0x3a000000, v240
	v_mul_f32_e32 v2, 0x4f800000, v1
	v_cmp_gt_f32_e32 vcc, s82, v1
	s_nop 1
	v_cndmask_b32_e32 v1, v1, v2, vcc
	v_sqrt_f32_e32 v2, v1
	s_nop 0
	v_add_u32_e32 v36, -1, v2
	v_fma_f32 v38, -v36, v2, v1
	v_add_u32_e32 v37, 1, v2
	v_cmp_ge_f32_e64 s[40:41], 0, v38
	s_nop 1
	v_cndmask_b32_e64 v36, v2, v36, s[40:41]
	v_fma_f32 v2, -v37, v2, v1
	v_cmp_lt_f32_e64 s[40:41], 0, v2
	s_nop 1
	v_cndmask_b32_e64 v2, v36, v37, s[40:41]
	v_mul_f32_e32 v36, 0x37800000, v2
	v_cndmask_b32_e32 v2, v2, v36, vcc
	v_cmp_class_f32_e32 vcc, v1, v241
	v_mul_f32_e32 v37, 0x3c010204, v110
	s_nop 0
	v_cndmask_b32_e32 v1, v2, v1, vcc
	v_div_scale_f32 v2, s[18:19], v1, v1, 1.0
	v_rcp_f32_e32 v36, v2
	s_add_u32 s18, s84, s42
	s_addc_u32 s19, s85, s43
	v_fma_f32 v38, -v2, v36, 1.0
	v_fmac_f32_e32 v36, v38, v36
	v_div_scale_f32 v38, vcc, 1.0, v1, 1.0
	v_mul_f32_e32 v39, v38, v36
	v_fma_f32 v40, -v2, v39, v38
	v_fmac_f32_e32 v39, v40, v36
	v_fma_f32 v2, -v2, v39, v38
	v_div_fmas_f32 v2, v2, v36, v39
	v_div_fixup_f32 v1, v2, v1, 1.0
	global_store_dword v236, v1, s[18:19]
	v_mul_f32_e32 v1, v1, v37
	global_store_dword v237, v1, s[18:19]
	s_branch .LBB0_1362
